# speedup vs baseline: 1.0121x; 1.0008x over previous
.Lg1_loop:
	ds_read_b128 v[152:155], v94
	ds_read_b128 v[136:139], v92
	ds_read_b128 v[156:159], v94 offset:2048
	ds_read_b128 v[140:143], v92 offset:2048
	ds_read_b128 v[160:163], v94 offset:4096
	ds_read_b128 v[144:147], v92 offset:4096
	s_add_i32 s18, s16, 3
	s_lshl_b32 s18, s18, 7
	s_add_u32 s22, s12, s18
	s_addc_u32 s23, s13, 0
	s_add_u32 s24, s14, s18
	s_addc_u32 s25, s15, 0
	s_add_i32 s26, s17, s20
	s_add_i32 s30, s26, s29
	s_add_i32 s27, s17, 0xd000
	s_cmp_lg_u32 s27, 0x27000
	s_cselect_b32 s27, s27, 0
	s_waitcnt lgkmcnt(6)
	v_mfma_f32_16x16x32_f16 v[34:37], v[116:119], v[100:103], v[34:37]
	v_mfma_f32_16x16x32_f16 v[78:81], v[120:123], v[100:103], v[78:81]
	ds_read_b128 v[164:167], v94 offset:6144
	v_mfma_f32_16x16x32_f16 v[74:77], v[124:127], v[100:103], v[74:77]
	ds_read_b128 v[148:151], v92 offset:6144
	v_mfma_f32_16x16x32_f16 v[70:73], v[128:131], v[100:103], v[70:73]
	ds_read_b128 v[168:171], v94 offset:8192
	v_mfma_f32_16x16x32_f16 v[62:65], v[132:135], v[100:103], v[62:65]
	v_mfma_f32_16x16x32_f16 v[58:61], v[116:119], v[104:107], v[58:61]
	v_mfma_f32_16x16x32_f16 v[54:57], v[120:123], v[104:107], v[54:57]
	v_add_u32_e32 v91, s27, v89
	v_mfma_f32_16x16x32_f16 v[50:53], v[124:127], v[104:107], v[50:53]
	v_mfma_f32_16x16x32_f16 v[46:49], v[128:131], v[104:107], v[46:49]
	v_add_u32_e32 v93, s27, v90
	v_mfma_f32_16x16x32_f16 v[42:45], v[132:135], v[104:107], v[42:45]
	v_mfma_f32_16x16x32_f16 v[38:41], v[116:119], v[108:111], v[38:41]
	v_xor_b32_e32 v92, 64, v91
	v_mfma_f32_16x16x32_f16 v[30:33], v[120:123], v[108:111], v[30:33]
	v_mfma_f32_16x16x32_f16 v[26:29], v[124:127], v[108:111], v[26:29]
	v_xor_b32_e32 v94, 64, v93
	v_mfma_f32_16x16x32_f16 v[22:25], v[128:131], v[108:111], v[22:25]
	v_mfma_f32_16x16x32_f16 v[18:21], v[132:135], v[108:111], v[18:21]
	v_mfma_f32_16x16x32_f16 v[14:17], v[116:119], v[112:115], v[14:17]
	v_mfma_f32_16x16x32_f16 v[10:13], v[120:123], v[112:115], v[10:13]
	v_mfma_f32_16x16x32_f16 v[2:5], v[124:127], v[112:115], v[2:5]
	v_mfma_f32_16x16x32_f16 v[6:9], v[128:131], v[112:115], v[6:9]
	v_mfma_f32_16x16x32_f16 v[66:69], v[132:135], v[112:115], v[66:69]
	s_waitcnt vmcnt(7)
	s_waitcnt lgkmcnt(0)
	s_barrier
	ds_read_b128 v[116:119], v93
	ds_read_b128 v[100:103], v91
	ds_read_b128 v[120:123], v93 offset:2048
	ds_read_b128 v[104:107], v91 offset:2048
	ds_read_b128 v[124:127], v93 offset:4096
	ds_read_b128 v[108:111], v91 offset:4096
	ds_read_b128 v[128:131], v93 offset:6144
	ds_read_b128 v[112:115], v91 offset:6144
	ds_read_b128 v[132:135], v93 offset:8192
	v_mfma_f32_16x16x32_f16 v[34:37], v[152:155], v[136:139], v[34:37]
	v_mfma_f32_16x16x32_f16 v[78:81], v[156:159], v[136:139], v[78:81]
	s_mov_b32 m0, s26
	s_add_i32 s26, s26, 0x2000
	global_load_lds_dwordx4 v82, s[22:23]
	v_mfma_f32_16x16x32_f16 v[74:77], v[160:163], v[136:139], v[74:77]
	v_mfma_f32_16x16x32_f16 v[70:73], v[164:167], v[136:139], v[70:73]
	s_mov_b32 m0, s26
	s_add_i32 s26, s26, 0x2000
	global_load_lds_dwordx4 v83, s[22:23]
	v_mfma_f32_16x16x32_f16 v[62:65], v[168:171], v[136:139], v[62:65]
	v_mfma_f32_16x16x32_f16 v[58:61], v[152:155], v[140:143], v[58:61]
	s_mov_b32 m0, s26
	s_add_i32 s26, s26, 0x2000
	global_load_lds_dwordx4 v84, s[22:23]
	v_mfma_f32_16x16x32_f16 v[54:57], v[156:159], v[140:143], v[54:57]
	v_mfma_f32_16x16x32_f16 v[50:53], v[160:163], v[140:143], v[50:53]
	s_mov_b32 m0, s26
	s_add_i32 s26, s26, 0x2000
	global_load_lds_dwordx4 v85, s[22:23]
	v_mfma_f32_16x16x32_f16 v[46:49], v[164:167], v[140:143], v[46:49]
	v_mfma_f32_16x16x32_f16 v[42:45], v[168:171], v[140:143], v[42:45]
	s_mov_b32 m0, s26
	s_add_i32 s26, s26, 0x2000
	global_load_lds_dwordx4 v86, s[24:25]
	v_mfma_f32_16x16x32_f16 v[38:41], v[152:155], v[144:147], v[38:41]
	v_mfma_f32_16x16x32_f16 v[30:33], v[156:159], v[144:147], v[30:33]
	s_mov_b32 m0, s26
	s_add_i32 s26, s26, 0x2000
	global_load_lds_dwordx4 v87, s[24:25]
	v_mfma_f32_16x16x32_f16 v[26:29], v[160:163], v[144:147], v[26:29]
	v_mfma_f32_16x16x32_f16 v[22:25], v[164:167], v[144:147], v[22:25]
	s_mov_b32 m0, s30
	s_nop 0
	global_load_lds_dwordx4 v88, s[24:25]
	v_mfma_f32_16x16x32_f16 v[18:21], v[168:171], v[144:147], v[18:21]
	v_mfma_f32_16x16x32_f16 v[14:17], v[152:155], v[148:151], v[14:17]
	v_mfma_f32_16x16x32_f16 v[10:13], v[156:159], v[148:151], v[10:13]
	v_mfma_f32_16x16x32_f16 v[2:5], v[160:163], v[148:151], v[2:5]
	v_mfma_f32_16x16x32_f16 v[6:9], v[164:167], v[148:151], v[6:9]
	v_mfma_f32_16x16x32_f16 v[66:69], v[168:171], v[148:151], v[66:69]
	s_mov_b32 s17, s27
	s_add_i32 s16, s16, 1
	s_cmp_lt_u32 s16, 13
	s_cbranch_scc1 .Lg1_loop
	ds_read_b128 v[152:155], v94
	ds_read_b128 v[136:139], v92
	ds_read_b128 v[156:159], v94 offset:2048
	ds_read_b128 v[140:143], v92 offset:2048
	ds_read_b128 v[160:163], v94 offset:4096
	ds_read_b128 v[144:147], v92 offset:4096
	s_add_i32 s27, s17, 0xd000
	s_cmp_lg_u32 s27, 0x27000
	s_cselect_b32 s27, s27, 0
	s_waitcnt lgkmcnt(6)
	v_mfma_f32_16x16x32_f16 v[34:37], v[116:119], v[100:103], v[34:37]
	v_mfma_f32_16x16x32_f16 v[78:81], v[120:123], v[100:103], v[78:81]
	ds_read_b128 v[164:167], v94 offset:6144
	v_mfma_f32_16x16x32_f16 v[74:77], v[124:127], v[100:103], v[74:77]
	ds_read_b128 v[148:151], v92 offset:6144
	v_mfma_f32_16x16x32_f16 v[70:73], v[128:131], v[100:103], v[70:73]
	ds_read_b128 v[168:171], v94 offset:8192
	v_mfma_f32_16x16x32_f16 v[62:65], v[132:135], v[100:103], v[62:65]
	v_mfma_f32_16x16x32_f16 v[58:61], v[116:119], v[104:107], v[58:61]
	v_mfma_f32_16x16x32_f16 v[54:57], v[120:123], v[104:107], v[54:57]
	v_add_u32_e32 v91, s27, v89
	v_mfma_f32_16x16x32_f16 v[50:53], v[124:127], v[104:107], v[50:53]
	v_mfma_f32_16x16x32_f16 v[46:49], v[128:131], v[104:107], v[46:49]
	v_add_u32_e32 v93, s27, v90
	v_mfma_f32_16x16x32_f16 v[42:45], v[132:135], v[104:107], v[42:45]
	v_mfma_f32_16x16x32_f16 v[38:41], v[116:119], v[108:111], v[38:41]
	v_xor_b32_e32 v92, 64, v91
	v_mfma_f32_16x16x32_f16 v[30:33], v[120:123], v[108:111], v[30:33]
	v_mfma_f32_16x16x32_f16 v[26:29], v[124:127], v[108:111], v[26:29]
	v_xor_b32_e32 v94, 64, v93
	v_mfma_f32_16x16x32_f16 v[22:25], v[128:131], v[108:111], v[22:25]
	v_mfma_f32_16x16x32_f16 v[18:21], v[132:135], v[108:111], v[18:21]
	v_mfma_f32_16x16x32_f16 v[14:17], v[116:119], v[112:115], v[14:17]
	v_mfma_f32_16x16x32_f16 v[10:13], v[120:123], v[112:115], v[10:13]
	v_mfma_f32_16x16x32_f16 v[2:5], v[124:127], v[112:115], v[2:5]
	v_mfma_f32_16x16x32_f16 v[6:9], v[128:131], v[112:115], v[6:9]
	v_mfma_f32_16x16x32_f16 v[66:69], v[132:135], v[112:115], v[66:69]
	s_waitcnt vmcnt(7)
	s_waitcnt lgkmcnt(0)
	s_barrier
	ds_read_b128 v[116:119], v93
	ds_read_b128 v[100:103], v91
	ds_read_b128 v[120:123], v93 offset:2048
	ds_read_b128 v[104:107], v91 offset:2048
	ds_read_b128 v[124:127], v93 offset:4096
	ds_read_b128 v[108:111], v91 offset:4096
	ds_read_b128 v[128:131], v93 offset:6144
	ds_read_b128 v[112:115], v91 offset:6144
	ds_read_b128 v[132:135], v93 offset:8192
	v_mfma_f32_16x16x32_f16 v[34:37], v[152:155], v[136:139], v[34:37]
	v_mfma_f32_16x16x32_f16 v[78:81], v[156:159], v[136:139], v[78:81]
	v_mfma_f32_16x16x32_f16 v[74:77], v[160:163], v[136:139], v[74:77]
	v_mfma_f32_16x16x32_f16 v[70:73], v[164:167], v[136:139], v[70:73]
	v_mfma_f32_16x16x32_f16 v[62:65], v[168:171], v[136:139], v[62:65]
	v_mfma_f32_16x16x32_f16 v[58:61], v[152:155], v[140:143], v[58:61]
	v_mfma_f32_16x16x32_f16 v[54:57], v[156:159], v[140:143], v[54:57]
	v_mfma_f32_16x16x32_f16 v[50:53], v[160:163], v[140:143], v[50:53]
	v_mfma_f32_16x16x32_f16 v[46:49], v[164:167], v[140:143], v[46:49]
	v_mfma_f32_16x16x32_f16 v[42:45], v[168:171], v[140:143], v[42:45]
	v_mfma_f32_16x16x32_f16 v[38:41], v[152:155], v[144:147], v[38:41]
	v_mfma_f32_16x16x32_f16 v[30:33], v[156:159], v[144:147], v[30:33]
	v_mfma_f32_16x16x32_f16 v[26:29], v[160:163], v[144:147], v[26:29]
	v_mfma_f32_16x16x32_f16 v[22:25], v[164:167], v[144:147], v[22:25]
	v_mfma_f32_16x16x32_f16 v[18:21], v[168:171], v[144:147], v[18:21]
	v_mfma_f32_16x16x32_f16 v[14:17], v[152:155], v[148:151], v[14:17]
	v_mfma_f32_16x16x32_f16 v[10:13], v[156:159], v[148:151], v[10:13]
	v_mfma_f32_16x16x32_f16 v[2:5], v[160:163], v[148:151], v[2:5]
	v_mfma_f32_16x16x32_f16 v[6:9], v[164:167], v[148:151], v[6:9]
	v_mfma_f32_16x16x32_f16 v[66:69], v[168:171], v[148:151], v[66:69]
	s_mov_b32 s17, s27
	ds_read_b128 v[152:155], v94
	ds_read_b128 v[136:139], v92
	ds_read_b128 v[156:159], v94 offset:2048
	ds_read_b128 v[140:143], v92 offset:2048
	ds_read_b128 v[160:163], v94 offset:4096
	ds_read_b128 v[144:147], v92 offset:4096
	s_add_i32 s27, s17, 0xd000
	s_cmp_lg_u32 s27, 0x27000
	s_cselect_b32 s27, s27, 0
	s_waitcnt lgkmcnt(6)
	v_mfma_f32_16x16x32_f16 v[34:37], v[116:119], v[100:103], v[34:37]
	v_mfma_f32_16x16x32_f16 v[78:81], v[120:123], v[100:103], v[78:81]
	ds_read_b128 v[164:167], v94 offset:6144
	v_mfma_f32_16x16x32_f16 v[74:77], v[124:127], v[100:103], v[74:77]
	ds_read_b128 v[148:151], v92 offset:6144
	v_mfma_f32_16x16x32_f16 v[70:73], v[128:131], v[100:103], v[70:73]
	ds_read_b128 v[168:171], v94 offset:8192
	v_mfma_f32_16x16x32_f16 v[62:65], v[132:135], v[100:103], v[62:65]
	v_mfma_f32_16x16x32_f16 v[58:61], v[116:119], v[104:107], v[58:61]
	v_mfma_f32_16x16x32_f16 v[54:57], v[120:123], v[104:107], v[54:57]
	v_add_u32_e32 v91, s27, v89
	v_mfma_f32_16x16x32_f16 v[50:53], v[124:127], v[104:107], v[50:53]
	v_mfma_f32_16x16x32_f16 v[46:49], v[128:131], v[104:107], v[46:49]
	v_add_u32_e32 v93, s27, v90
	v_mfma_f32_16x16x32_f16 v[42:45], v[132:135], v[104:107], v[42:45]
	v_mfma_f32_16x16x32_f16 v[38:41], v[116:119], v[108:111], v[38:41]
	v_xor_b32_e32 v92, 64, v91
	v_mfma_f32_16x16x32_f16 v[30:33], v[120:123], v[108:111], v[30:33]
	v_mfma_f32_16x16x32_f16 v[26:29], v[124:127], v[108:111], v[26:29]
	v_xor_b32_e32 v94, 64, v93
	v_mfma_f32_16x16x32_f16 v[22:25], v[128:131], v[108:111], v[22:25]
	v_mfma_f32_16x16x32_f16 v[18:21], v[132:135], v[108:111], v[18:21]
	v_mfma_f32_16x16x32_f16 v[14:17], v[116:119], v[112:115], v[14:17]
	v_mfma_f32_16x16x32_f16 v[10:13], v[120:123], v[112:115], v[10:13]
	v_mfma_f32_16x16x32_f16 v[2:5], v[124:127], v[112:115], v[2:5]
	v_mfma_f32_16x16x32_f16 v[6:9], v[128:131], v[112:115], v[6:9]
	v_mfma_f32_16x16x32_f16 v[66:69], v[132:135], v[112:115], v[66:69]
	s_waitcnt vmcnt(0)
	s_waitcnt lgkmcnt(0)
	s_barrier
	ds_read_b128 v[116:119], v93
	ds_read_b128 v[100:103], v91
	ds_read_b128 v[120:123], v93 offset:2048
	ds_read_b128 v[104:107], v91 offset:2048
	ds_read_b128 v[124:127], v93 offset:4096
	ds_read_b128 v[108:111], v91 offset:4096
	ds_read_b128 v[128:131], v93 offset:6144
	ds_read_b128 v[112:115], v91 offset:6144
	ds_read_b128 v[132:135], v93 offset:8192
	v_mfma_f32_16x16x32_f16 v[34:37], v[152:155], v[136:139], v[34:37]
	v_mfma_f32_16x16x32_f16 v[78:81], v[156:159], v[136:139], v[78:81]
	v_mfma_f32_16x16x32_f16 v[74:77], v[160:163], v[136:139], v[74:77]
	v_mfma_f32_16x16x32_f16 v[70:73], v[164:167], v[136:139], v[70:73]
	v_mfma_f32_16x16x32_f16 v[62:65], v[168:171], v[136:139], v[62:65]
	v_mfma_f32_16x16x32_f16 v[58:61], v[152:155], v[140:143], v[58:61]
	v_mfma_f32_16x16x32_f16 v[54:57], v[156:159], v[140:143], v[54:57]
	v_mfma_f32_16x16x32_f16 v[50:53], v[160:163], v[140:143], v[50:53]
	v_mfma_f32_16x16x32_f16 v[46:49], v[164:167], v[140:143], v[46:49]
	v_mfma_f32_16x16x32_f16 v[42:45], v[168:171], v[140:143], v[42:45]
	v_mfma_f32_16x16x32_f16 v[38:41], v[152:155], v[144:147], v[38:41]
	v_mfma_f32_16x16x32_f16 v[30:33], v[156:159], v[144:147], v[30:33]
	v_mfma_f32_16x16x32_f16 v[26:29], v[160:163], v[144:147], v[26:29]
	v_mfma_f32_16x16x32_f16 v[22:25], v[164:167], v[144:147], v[22:25]
	v_mfma_f32_16x16x32_f16 v[18:21], v[168:171], v[144:147], v[18:21]
	v_mfma_f32_16x16x32_f16 v[14:17], v[152:155], v[148:151], v[14:17]
	v_mfma_f32_16x16x32_f16 v[10:13], v[156:159], v[148:151], v[10:13]
	v_mfma_f32_16x16x32_f16 v[2:5], v[160:163], v[148:151], v[2:5]
	v_mfma_f32_16x16x32_f16 v[6:9], v[164:167], v[148:151], v[6:9]
	v_mfma_f32_16x16x32_f16 v[66:69], v[168:171], v[148:151], v[66:69]
	s_mov_b32 s17, s27
	ds_read_b128 v[152:155], v94
	ds_read_b128 v[136:139], v92
	ds_read_b128 v[156:159], v94 offset:2048
	ds_read_b128 v[140:143], v92 offset:2048
	ds_read_b128 v[160:163], v94 offset:4096
	ds_read_b128 v[144:147], v92 offset:4096
	s_add_i32 s27, s17, 0xd000
	s_cmp_lg_u32 s27, 0x27000
	s_cselect_b32 s27, s27, 0
	s_waitcnt lgkmcnt(6)
	v_mfma_f32_16x16x32_f16 v[34:37], v[116:119], v[100:103], v[34:37]
	v_mfma_f32_16x16x32_f16 v[78:81], v[120:123], v[100:103], v[78:81]
	ds_read_b128 v[164:167], v94 offset:6144
	v_mfma_f32_16x16x32_f16 v[74:77], v[124:127], v[100:103], v[74:77]
	ds_read_b128 v[148:151], v92 offset:6144
	v_mfma_f32_16x16x32_f16 v[70:73], v[128:131], v[100:103], v[70:73]
	ds_read_b128 v[168:171], v94 offset:8192
	v_mfma_f32_16x16x32_f16 v[62:65], v[132:135], v[100:103], v[62:65]
	v_mfma_f32_16x16x32_f16 v[58:61], v[116:119], v[104:107], v[58:61]
	v_mfma_f32_16x16x32_f16 v[54:57], v[120:123], v[104:107], v[54:57]
	v_add_u32_e32 v91, s27, v89
	v_mfma_f32_16x16x32_f16 v[50:53], v[124:127], v[104:107], v[50:53]
	v_mfma_f32_16x16x32_f16 v[46:49], v[128:131], v[104:107], v[46:49]
	v_add_u32_e32 v93, s27, v90
	v_mfma_f32_16x16x32_f16 v[42:45], v[132:135], v[104:107], v[42:45]
	v_mfma_f32_16x16x32_f16 v[38:41], v[116:119], v[108:111], v[38:41]
	v_xor_b32_e32 v92, 64, v91
	v_mfma_f32_16x16x32_f16 v[30:33], v[120:123], v[108:111], v[30:33]
	v_mfma_f32_16x16x32_f16 v[26:29], v[124:127], v[108:111], v[26:29]
	v_xor_b32_e32 v94, 64, v93
	v_mfma_f32_16x16x32_f16 v[22:25], v[128:131], v[108:111], v[22:25]
	v_mfma_f32_16x16x32_f16 v[18:21], v[132:135], v[108:111], v[18:21]
	v_mfma_f32_16x16x32_f16 v[14:17], v[116:119], v[112:115], v[14:17]
	v_mfma_f32_16x16x32_f16 v[10:13], v[120:123], v[112:115], v[10:13]
	v_mfma_f32_16x16x32_f16 v[2:5], v[124:127], v[112:115], v[2:5]
	v_mfma_f32_16x16x32_f16 v[6:9], v[128:131], v[112:115], v[6:9]
	v_mfma_f32_16x16x32_f16 v[66:69], v[132:135], v[112:115], v[66:69]
	s_waitcnt lgkmcnt(0)
	s_barrier
	ds_read_b128 v[116:119], v93
	ds_read_b128 v[100:103], v91
	ds_read_b128 v[120:123], v93 offset:2048
	ds_read_b128 v[104:107], v91 offset:2048
	ds_read_b128 v[124:127], v93 offset:4096
	ds_read_b128 v[108:111], v91 offset:4096
	ds_read_b128 v[128:131], v93 offset:6144
	ds_read_b128 v[112:115], v91 offset:6144
	ds_read_b128 v[132:135], v93 offset:8192
	v_mfma_f32_16x16x32_f16 v[34:37], v[152:155], v[136:139], v[34:37]
	v_mfma_f32_16x16x32_f16 v[78:81], v[156:159], v[136:139], v[78:81]
	v_mfma_f32_16x16x32_f16 v[74:77], v[160:163], v[136:139], v[74:77]
	v_mfma_f32_16x16x32_f16 v[70:73], v[164:167], v[136:139], v[70:73]
	v_mfma_f32_16x16x32_f16 v[62:65], v[168:171], v[136:139], v[62:65]
	v_mfma_f32_16x16x32_f16 v[58:61], v[152:155], v[140:143], v[58:61]
	v_mfma_f32_16x16x32_f16 v[54:57], v[156:159], v[140:143], v[54:57]
	v_mfma_f32_16x16x32_f16 v[50:53], v[160:163], v[140:143], v[50:53]
	v_mfma_f32_16x16x32_f16 v[46:49], v[164:167], v[140:143], v[46:49]
	v_mfma_f32_16x16x32_f16 v[42:45], v[168:171], v[140:143], v[42:45]
	v_mfma_f32_16x16x32_f16 v[38:41], v[152:155], v[144:147], v[38:41]
	v_mfma_f32_16x16x32_f16 v[30:33], v[156:159], v[144:147], v[30:33]
	v_mfma_f32_16x16x32_f16 v[26:29], v[160:163], v[144:147], v[26:29]
	v_mfma_f32_16x16x32_f16 v[22:25], v[164:167], v[144:147], v[22:25]
	v_mfma_f32_16x16x32_f16 v[18:21], v[168:171], v[144:147], v[18:21]
	v_mfma_f32_16x16x32_f16 v[14:17], v[152:155], v[148:151], v[14:17]
	v_mfma_f32_16x16x32_f16 v[10:13], v[156:159], v[148:151], v[10:13]
	v_mfma_f32_16x16x32_f16 v[2:5], v[160:163], v[148:151], v[2:5]
	v_mfma_f32_16x16x32_f16 v[6:9], v[164:167], v[148:151], v[6:9]
	v_mfma_f32_16x16x32_f16 v[66:69], v[168:171], v[148:151], v[66:69]
	s_mov_b32 s17, s27
	s_nop 7
